# helper share 14x171 runs
# baseline (speedup 1.0000x reference)
; #define LDS_AS __attribute__((address_space(3)))
; #define OPAQUE_TID(P) (((P).wid0 << 6) | lane_id_now())
; #define LAS __attribute__((address_space(3)))
; template <int NS, bool STREAM_ONLY = false>
; DI void convert_experts_dma(const Params& p, LDS_AS unsigned char* lds, int bid, int nb) {
;   const int tid = OPAQUE_TID(p), wid = __builtin_amdgcn_readfirstlane(tid >> 6), lane = tid & 63;
;   constexpr int NT = 32 * 1536;
;   const int nvalid = bid < NT / CVG ? CVG * ((NT / CVG - bid + nb - 1) / nb) : 0;
; __global__ void __launch_bounds__(NTHREADS, 2) k_forward(Params p_in) {
;     ...
;   if (is_cv) {
;     {
;       volatile LAS unsigned* stw = (volatile LAS unsigned*)dyn_smem;
;       const unsigned s0 = stw[0], s1 = stw[1];
;       __syncthreads();
;       convert_experts_dma<5>(p, (LDS_AS unsigned char*)dyn_smem, cvid, ncv);
.LBB0_1119:
	s_or_b64 exec, exec, s[0:1]
	s_mov_b64 s[12:13], 0
	s_mov_b32 s20, 0
	s_mov_b64 s[0:1], 0
	v_readlane_b32 s97, v255, 13
	s_mov_b32 s99, s96
	s_nop 0
	s_mov_b32 s98, s97
	s_cmp_lg_u32 s55, 0
	s_cbranch_scc0 .LBB0_1181
	v_readlane_b32 s98, v255, 17
	s_sub_i32 s99, s96, s55
	s_add_i32 s98, s98, 0x26a6
	s_branch .LBB0_1181
.LBB0_1121:
	v_mov_b32_e32 v0, 0
	ds_read_b32 v2, v0
	ds_read_b32 v3, v0 offset:4
	s_waitcnt lgkmcnt(0)
	s_barrier
	v_mbcnt_lo_u32_b32 v0, -1, 0
	v_mbcnt_hi_u32_b32 v0, -1, v0
	s_mov_b32 s6, 0
	v_or_b32_e32 v1, s87, v0
	s_cmpk_gt_i32 s54, 0x26a5
	v_readfirstlane_b32 s0, v1
	s_mov_b32 s18, 0
	s_cbranch_scc1 .LBB0_1123
	s_abs_i32 s1, s55
	v_cvt_f32_u32_e32 v1, s1
	s_sub_i32 s2, s55, s54
	s_add_i32 s3, s2, 0x26a5
	s_sub_i32 s2, 0xffffd95b, s2
	v_rcp_iflag_f32_e32 v1, v1
	s_xor_b32 s5, s3, s55
	s_sub_i32 s4, 0, s1
	s_max_i32 s2, s3, s2
	v_mul_f32_e32 v1, 0x4f7ffffe, v1
	v_cvt_u32_f32_e32 v1, v1
	s_ashr_i32 s3, s5, 31
	v_readfirstlane_b32 s5, v1
	s_mul_i32 s4, s4, s5
	s_mul_hi_u32 s4, s5, s4
	s_add_i32 s5, s5, s4
	s_mul_hi_u32 s4, s2, s5
	s_mul_i32 s5, s4, s1
	s_sub_i32 s2, s2, s5
	s_add_i32 s7, s4, 1
	s_sub_i32 s5, s2, s1
	s_cmp_ge_u32 s2, s1
	s_cselect_b32 s4, s7, s4
	s_cselect_b32 s2, s5, s2
	s_add_i32 s5, s4, 1
	s_cmp_ge_u32 s2, s1
	s_cselect_b32 s1, s5, s4
	s_xor_b32 s1, s1, s3
	s_sub_i32 s1, s1, s3
	s_lshl_b32 s18, s1, 2
